# k_sort fetches its own code lines at entry under the kernarg/input latency
# speedup vs baseline: 1.0020x; 1.0020x over previous
_Z6k_sortPKfS0_PKiS2_PiP15HIP_vector_typeIfLj4EEPfS7_S3_S7_S7_S3_S3_S6_S6_:
	s_getpc_b64 s[52:53]
	v_lshlrev_b32_e32 v43, 6, v0
	v_min_u32_e32 v43, 0xf00, v43
	global_load_dword v43, v43, s[52:53]
	s_load_dwordx2 s[4:5], s[0:1], 0x70
	s_load_dwordx8 s[8:15], s[0:1], 0x0
	s_load_dwordx8 s[36:43], s[0:1], 0x40
	s_load_dwordx2 s[44:45], s[0:1], 0x60
	s_load_dwordx2 s[46:47], s[0:1], 0x20
	s_load_dwordx4 s[48:51], s[0:1], 0x30
	s_mov_b32 s17, 0
	s_mov_b32 s16, s17
	v_lshl_or_b32 v2, s2, 12, v0
	v_mov_b32_e32 v3, 0
	s_mov_b32 s18, s17
	s_mov_b32 s19, s17
	v_mov_b64_e32 v[6:7], s[16:17]
	s_waitcnt lgkmcnt(0)
	v_lshl_add_u64 v[4:5], v[2:3], 4, s[4:5]
	v_mov_b64_e32 v[8:9], s[18:19]
	global_store_dwordx4 v[4:5], v[6:9], off
	v_or_b32_e32 v4, 0x400, v2
	v_mov_b32_e32 v5, v3
	v_lshl_add_u64 v[4:5], v[4:5], 4, s[4:5]
	global_store_dwordx4 v[4:5], v[6:9], off
	v_or_b32_e32 v4, 0x800, v2
	v_mov_b32_e32 v5, v3
	v_lshl_add_u64 v[4:5], v[4:5], 4, s[4:5]
	v_or_b32_e32 v2, 0xc00, v2
	s_movk_i32 s3, 0x100
	global_store_dwordx4 v[4:5], v[6:9], off
	v_lshl_add_u64 v[4:5], v[2:3], 4, s[4:5]
	v_cmp_gt_u32_e64 s[6:7], s3, v0
	global_store_dwordx4 v[4:5], v[6:9], off
	s_and_saveexec_b64 s[4:5], s[6:7]
	v_mov_b32_e32 v1, 0x10400
	v_lshl_add_u32 v1, v0, 2, v1
	ds_write_b32 v1, v3
	s_or_b64 exec, exec, s[4:5]
	s_lshr_b32 s28, s2, 1
	s_and_b32 s18, s2, 1
	s_bitcmp1_b32 s2, 0
	s_cselect_b64 s[2:3], -1, 0
	s_lshl_b32 s16, s28, 12
	s_lshl_b64 s[4:5], s[16:17], 3
	s_cmp_eq_u32 s18, 0
	s_cselect_b32 s8, s8, s10
	s_cselect_b32 s9, s9, s11
	s_cselect_b32 s10, s12, s14
	s_cselect_b32 s11, s13, s15
	s_add_u32 s4, s8, s4
	v_or_b32_e32 v13, 0x400, v0
	s_addc_u32 s5, s9, s5
	v_lshlrev_b32_e32 v1, 3, v0
	v_lshlrev_b32_e32 v2, 3, v13
	v_or_b32_e32 v12, 0x800, v0
	global_load_dwordx2 v[8:9], v1, s[4:5]
	global_load_dwordx2 v[4:5], v2, s[4:5]
	v_lshlrev_b32_e32 v2, 3, v12
	v_or_b32_e32 v10, 0xc00, v0
	global_load_dwordx2 v[6:7], v2, s[4:5]
	v_lshlrev_b32_e32 v2, 3, v10
	global_load_dwordx2 v[2:3], v2, s[4:5]
	s_lshl_b64 s[4:5], s[16:17], 2
	s_add_u32 s4, s10, s4
	s_addc_u32 s5, s11, s5
	v_lshlrev_b32_e32 v11, 2, v0
	v_lshlrev_b32_e32 v14, 2, v13
	global_load_dword v17, v11, s[4:5]
	global_load_dword v16, v14, s[4:5]
	v_lshlrev_b32_e32 v14, 2, v12
	global_load_dword v15, v14, s[4:5]
	v_lshlrev_b32_e32 v14, 2, v10
	global_load_dword v14, v14, s[4:5]
	v_mov_b32_e32 v20, 0
	ds_write2st64_b32 v11, v20, v20 offset0:192 offset1:208
	ds_write2st64_b32 v11, v20, v20 offset0:224 offset1:240
	v_mov_b32_e32 v18, 0xff
	v_mov_b32_e32 v25, 0x10400
	v_mov_b32_e32 v19, 1
	s_waitcnt lgkmcnt(0)
	s_barrier
	v_cmp_gt_u32_e32 vcc, 64, v0
	s_waitcnt vmcnt(7)
	v_mul_f32_e32 v20, 0x43800000, v8
	s_waitcnt vmcnt(6)
	v_mul_f32_e32 v21, 0x43800000, v4
	v_cvt_i32_f32_e32 v20, v20
	v_cvt_i32_f32_e32 v21, v21
	s_waitcnt vmcnt(5)
	v_mul_f32_e32 v22, 0x43800000, v6
	v_cvt_i32_f32_e32 v22, v22
	s_waitcnt vmcnt(4)
	v_mul_f32_e32 v23, 0x43800000, v2
	v_cvt_i32_f32_e32 v23, v23
	v_med3_i32 v26, v20, 0, v18
	v_med3_i32 v20, v21, 0, v18
	v_med3_i32 v22, v22, 0, v18
	v_med3_i32 v24, v23, 0, v18
	v_lshl_add_u32 v21, v26, 2, v25
	v_lshl_add_u32 v23, v20, 2, v25
	v_lshl_add_u32 v28, v22, 2, v25
	ds_add_rtn_u32 v27, v21, v19
	ds_add_rtn_u32 v21, v23, v19
	ds_add_rtn_u32 v23, v28, v19
	v_lshl_add_u32 v25, v24, 2, v25
	ds_add_rtn_u32 v25, v25, v19
	s_waitcnt lgkmcnt(0)
	s_barrier
	s_and_saveexec_b64 s[4:5], vcc
	s_cbranch_execz .LBB0_4
	v_lshlrev_b32_e32 v33, 4, v0
	v_add_u32_e32 v28, 0x10400, v33
	ds_read_b128 v[28:31], v28
	v_mov_b32_e32 v32, 0
	s_waitcnt lgkmcnt(0)
	v_add_u32_e32 v34, v29, v28
	v_add3_u32 v31, v34, v30, v31
	s_nop 1
	v_add_u32_dpp v34, v31, v31 row_shr:1 row_mask:0xf bank_mask:0xf bound_ctrl:1
	s_nop 1
	v_add_u32_dpp v34, v34, v34 row_shr:2 row_mask:0xf bank_mask:0xf bound_ctrl:1
	s_nop 1
	v_add_u32_dpp v34, v34, v34 row_shr:4 row_mask:0xf bank_mask:0xf bound_ctrl:1
	s_nop 1
	v_add_u32_dpp v34, v34, v34 row_shr:8 row_mask:0xf bank_mask:0xf bound_ctrl:1
	s_nop 1
	v_add_u32_dpp v34, v34, v34 row_bcast:15 row_mask:0xa bank_mask:0xf
	s_nop 1
	v_mov_b32_dpp v32, v34 row_bcast:31 row_mask:0xc bank_mask:0xf
	v_sub_u32_e32 v31, v32, v31
	v_add_u32_e32 v32, v31, v34
	v_or_b32_e32 v31, 0x10000, v33
	v_add_u32_e32 v33, v32, v28
	v_add_u32_e32 v34, v33, v29
	v_add_u32_e32 v35, v34, v30
	ds_write_b128 v31, v[32:35]

.LBB0_6:
	s_or_b64 exec, exec, s[4:5]
	s_waitcnt lgkmcnt(0)
	s_barrier
	ds_read_b32 v19, v29
	v_lshl_add_u32 v26, v26, s8, v27
	ds_read_b32 v27, v30
	ds_read_b32 v28, v28
	ds_read_b32 v25, v25
	s_waitcnt vmcnt(3)
	v_cmp_eq_u32_e32 vcc, 0, v17
	s_mov_b64 s[4:5], -1
	s_waitcnt lgkmcnt(3)
	v_add_lshl_u32 v19, v26, v19, 2
	ds_write2st64_b32 v19, v8, v9 offset1:64
	v_bfrev_b32_e32 v8, 1
	v_cndmask_b32_e32 v8, 0, v8, vcc
	v_or_b32_e32 v8, v8, v0
	ds_write_b32 v19, v8 offset:32768
	v_lshl_add_u32 v8, v20, s8, v21
	s_waitcnt lgkmcnt(4)
	v_add_lshl_u32 v8, v8, v27, 2
	ds_write2st64_b32 v8, v4, v5 offset1:64
	v_mov_b32_e32 v4, 0x400
	v_mov_b32_e32 v5, 0x80000400
	s_waitcnt vmcnt(2)
	v_cmp_eq_u32_e32 vcc, 0, v16
	s_nop 1
	v_cndmask_b32_e32 v4, v4, v5, vcc
	v_or_b32_e32 v4, v4, v0
	ds_write_b32 v8, v4 offset:32768
	v_lshl_add_u32 v4, v22, s8, v23
	s_waitcnt lgkmcnt(5)
	v_add_lshl_u32 v4, v4, v28, 2
	ds_write2st64_b32 v4, v6, v7 offset1:64
	v_mov_b32_e32 v5, 0x800
	v_mov_b32_e32 v6, 0x80000800
	s_waitcnt vmcnt(1)
	v_cmp_eq_u32_e32 vcc, 0, v15
	s_nop 1
	v_cndmask_b32_e32 v5, v5, v6, vcc
	v_or_b32_e32 v5, v5, v0
	ds_write_b32 v4, v5 offset:32768
	v_lshl_add_u32 v4, v24, s8, v18
	s_waitcnt lgkmcnt(6)
	v_add_lshl_u32 v4, v4, v25, 2
	ds_write2st64_b32 v4, v2, v3 offset1:64
	v_mov_b32_e32 v2, 0xc00
	v_mov_b32_e32 v3, 0x80000c00
	s_waitcnt vmcnt(0)
	v_cmp_eq_u32_e32 vcc, 0, v14
	s_nop 1
	v_cndmask_b32_e32 v2, v2, v3, vcc
	v_or_b32_e32 v2, v2, v0
	ds_write_b32 v4, v2 offset:32768
	s_waitcnt lgkmcnt(0)
	s_barrier
	s_getpc_b64 s[30:31]
	s_add_u32 s30, s30, 0x24a0
	s_addc_u32 s31, s31, 0
	v_lshlrev_b32_e32 v40, 6, v0
	v_min_u32_e32 v40, 0x2d00, v40
	global_load_dword v40, v40, s[30:31]
	s_and_b32 s32, s0, 0xfffff000
	s_mov_b32 s33, s1
	v_and_b32_e32 v41, 63, v0
	v_lshlrev_b32_e32 v41, 6, v41
	global_load_dword v41, v41, s[32:33]
	ds_read_b32 v14, v11 offset:32768
	s_mov_b64 s[18:19], s[44:45]
	s_mov_b64 s[8:9], s[36:37]
	s_mov_b64 s[10:11], s[38:39]
	s_mov_b64 s[12:13], s[40:41]
	s_mov_b64 s[14:15], s[42:43]
	ds_read2st64_b32 v[4:5], v11 offset1:64
	v_or_b32_e32 v2, s16, v0
	v_mov_b32_e32 v3, 0
	s_waitcnt lgkmcnt(0)
	v_and_b32_e32 v15, 0x7fffffff, v14
	s_and_b64 vcc, exec, s[2:3]
	v_lshlrev_b64 v[6:7], 2, v[2:3]
	s_cbranch_vccz .LBB0_8
	v_lshl_add_u64 v[8:9], s[10:11], 0, v[6:7]
	global_store_dword v[8:9], v4, off
	v_lshl_add_u64 v[8:9], s[12:13], 0, v[6:7]
	global_store_dword v[8:9], v5, off
	v_lshl_add_u64 v[8:9], s[14:15], 0, v[6:7]
	global_store_dword v[8:9], v15, off
	s_mov_b64 s[4:5], 0

	.amdhsa_kernel _Z6k_sortPKfS0_PKiS2_PiP15HIP_vector_typeIfLj4EEPfS7_S3_S7_S7_S3_S3_S6_S6_
		.amdhsa_group_segment_fixed_size 67584
		.amdhsa_private_segment_fixed_size 0
		.amdhsa_kernarg_size 120
		.amdhsa_user_sgpr_count 2
		.amdhsa_user_sgpr_dispatch_ptr 0
		.amdhsa_user_sgpr_queue_ptr 0
		.amdhsa_user_sgpr_kernarg_segment_ptr 1
		.amdhsa_user_sgpr_dispatch_id 0
		.amdhsa_user_sgpr_kernarg_preload_length 0
		.amdhsa_user_sgpr_kernarg_preload_offset 0
		.amdhsa_user_sgpr_private_segment_size 0
		.amdhsa_uses_dynamic_stack 0
		.amdhsa_enable_private_segment 0
		.amdhsa_system_sgpr_workgroup_id_x 1
		.amdhsa_system_sgpr_workgroup_id_y 0
		.amdhsa_system_sgpr_workgroup_id_z 0
		.amdhsa_system_sgpr_workgroup_info 0
		.amdhsa_system_vgpr_workitem_id 0
		.amdhsa_next_free_vgpr 48
		.amdhsa_next_free_sgpr 56
		.amdhsa_accum_offset 48
		.amdhsa_reserve_vcc 1
		.amdhsa_float_round_mode_32 0
		.amdhsa_float_round_mode_16_64 0
		.amdhsa_float_denorm_mode_32 3
		.amdhsa_float_denorm_mode_16_64 3
		.amdhsa_dx10_clamp 1
		.amdhsa_ieee_mode 1
		.amdhsa_fp16_overflow 0
		.amdhsa_tg_split 0
		.amdhsa_exception_fp_ieee_invalid_op 0
		.amdhsa_exception_fp_denorm_src 0
		.amdhsa_exception_fp_ieee_div_zero 0
		.amdhsa_exception_fp_ieee_overflow 0
		.amdhsa_exception_fp_ieee_underflow 0
		.amdhsa_exception_fp_ieee_inexact 0
		.amdhsa_exception_int_div_zero 0
	.end_amdhsa_kernel

amdhsa.kernels:
  - .agpr_count:     0
    .args:
      - .actual_access:  read_only
        .address_space:  global
        .offset:         0
        .size:           8
        .value_kind:     global_buffer
      - .actual_access:  read_only
        .address_space:  global
        .offset:         8
        .size:           8
        .value_kind:     global_buffer
      - .actual_access:  read_only
        .address_space:  global
        .offset:         16
        .size:           8
        .value_kind:     global_buffer
      - .actual_access:  read_only
        .address_space:  global
        .offset:         24
        .size:           8
        .value_kind:     global_buffer
      - .actual_access:  write_only
        .address_space:  global
        .offset:         32
        .size:           8
        .value_kind:     global_buffer
      - .actual_access:  write_only
        .address_space:  global
        .offset:         40
        .size:           8
        .value_kind:     global_buffer
      - .actual_access:  write_only
        .address_space:  global
        .offset:         48
        .size:           8
        .value_kind:     global_buffer
      - .actual_access:  write_only
        .address_space:  global
        .offset:         56
        .size:           8
        .value_kind:     global_buffer
      - .actual_access:  write_only
        .address_space:  global
        .offset:         64
        .size:           8
        .value_kind:     global_buffer
      - .actual_access:  write_only
        .address_space:  global
        .offset:         72
        .size:           8
        .value_kind:     global_buffer
      - .actual_access:  write_only
        .address_space:  global
        .offset:         80
        .size:           8
        .value_kind:     global_buffer
      - .actual_access:  write_only
        .address_space:  global
        .offset:         88
        .size:           8
        .value_kind:     global_buffer
      - .actual_access:  write_only
        .address_space:  global
        .offset:         96
        .size:           8
        .value_kind:     global_buffer
      - .actual_access:  write_only
        .address_space:  global
        .offset:         104
        .size:           8
        .value_kind:     global_buffer
      - .actual_access:  write_only
        .address_space:  global
        .offset:         112
        .size:           8
        .value_kind:     global_buffer
    .group_segment_fixed_size: 67584
    .kernarg_segment_align: 8
    .kernarg_segment_size: 120
    .language:       OpenCL C
    .language_version:
      - 2
      - 0
    .max_flat_workgroup_size: 1024
    .name:           _Z6k_sortPKfS0_PKiS2_PiP15HIP_vector_typeIfLj4EEPfS7_S3_S7_S7_S3_S3_S6_S6_
    .private_segment_fixed_size: 0
    .sgpr_count:     62
    .sgpr_spill_count: 0
    .symbol:         _Z6k_sortPKfS0_PKiS2_PiP15HIP_vector_typeIfLj4EEPfS7_S3_S7_S7_S3_S3_S6_S6_.kd
    .uniform_work_group_size: 1
    .uses_dynamic_stack: false
    .vgpr_count:     48
    .vgpr_spill_count: 0
    .wavefront_size: 64
  - .agpr_count:     0
    .args:
      - .actual_access:  read_only
        .address_space:  global
        .offset:         0
        .size:           8
        .value_kind:     global_buffer
      - .actual_access:  read_only
        .address_space:  global
        .offset:         8
        .size:           8
        .value_kind:     global_buffer
      - .actual_access:  read_only
        .address_space:  global
        .offset:         16
        .size:           8
        .value_kind:     global_buffer
      - .actual_access:  read_only
        .address_space:  global
        .offset:         24
        .size:           8
        .value_kind:     global_buffer
      - .actual_access:  read_only
        .address_space:  global
        .offset:         32
        .size:           8
        .value_kind:     global_buffer
      - .actual_access:  read_only
        .address_space:  global
        .offset:         40
        .size:           8
        .value_kind:     global_buffer
      - .actual_access:  read_only
        .address_space:  global
        .offset:         48
        .size:           8
        .value_kind:     global_buffer
      - .actual_access:  write_only
        .address_space:  global
        .offset:         56
        .size:           8
        .value_kind:     global_buffer
    .group_segment_fixed_size: 145952
    .kernarg_segment_align: 8
    .kernarg_segment_size: 64
    .language:       OpenCL C
    .language_version:
      - 2
      - 0
    .max_flat_workgroup_size: 512
    .name:           _Z7k_finalPK15HIP_vector_typeIfLj4EES2_PKiS4_PKfS6_PKDF16_Pf
    .private_segment_fixed_size: 0
    .sgpr_count:     34
    .sgpr_spill_count: 0
    .symbol:         _Z7k_finalPK15HIP_vector_typeIfLj4EES2_PKiS4_PKfS6_PKDF16_Pf.kd
    .uniform_work_group_size: 1
    .uses_dynamic_stack: false
    .vgpr_count:     177
    .vgpr_spill_count: 0
    .wavefront_size: 64
  - .agpr_count:     0
    .args:
      - .actual_access:  read_only
        .address_space:  global
        .offset:         0
        .size:           8
        .value_kind:     global_buffer
      - .actual_access:  read_only
        .address_space:  global
        .offset:         8
        .size:           8
        .value_kind:     global_buffer
      - .actual_access:  read_only
        .address_space:  global
        .offset:         16
        .size:           8
        .value_kind:     global_buffer
      - .actual_access:  read_only
        .address_space:  global
        .offset:         24
        .size:           8
        .value_kind:     global_buffer
      - .actual_access:  read_only
        .address_space:  global
        .offset:         32
        .size:           8
        .value_kind:     global_buffer
      - .actual_access:  read_only
        .address_space:  global
        .offset:         40
        .size:           8
        .value_kind:     global_buffer
      - .actual_access:  read_only
        .address_space:  global
        .offset:         48
        .size:           8
        .value_kind:     global_buffer
      - .actual_access:  read_only
        .address_space:  global
        .offset:         56
        .size:           8
        .value_kind:     global_buffer
      - .actual_access:  read_only
        .address_space:  global
        .offset:         64
        .size:           8
        .value_kind:     global_buffer
      - .address_space:  global
        .offset:         72
        .size:           8
        .value_kind:     global_buffer
      - .actual_access:  read_only
        .address_space:  global
        .offset:         80
        .size:           8
        .value_kind:     global_buffer
      - .actual_access:  read_only
        .address_space:  global
        .offset:         88
        .size:           8
        .value_kind:     global_buffer
      - .actual_access:  read_only
        .address_space:  global
        .offset:         96
        .size:           8
        .value_kind:     global_buffer
      - .actual_access:  write_only
        .address_space:  global
        .offset:         104
        .size:           8
        .value_kind:     global_buffer
      - .address_space:  global
        .offset:         112
        .size:           8
        .value_kind:     global_buffer
      - .actual_access:  write_only
        .address_space:  global
        .offset:         120
        .size:           8
        .value_kind:     global_buffer
      - .actual_access:  write_only
        .address_space:  global
        .offset:         128
        .size:           8
        .value_kind:     global_buffer
      - .actual_access:  write_only
        .address_space:  global
        .offset:         136
        .size:           8
        .value_kind:     global_buffer
      - .actual_access:  write_only
        .address_space:  global
        .offset:         144
        .size:           8
        .value_kind:     global_buffer
    .group_segment_fixed_size: 30384
    .kernarg_segment_align: 8
    .kernarg_segment_size: 152
    .language:       OpenCL C
    .language_version:
      - 2
      - 0
    .max_flat_workgroup_size: 512
    .name:           _Z6k_iterILb1ELb0EEvPKfS1_PKiPK15HIP_vector_typeIfLj4EES7_S1_S1_S3_S1_PfS8_S1_S3_PDF16_PS5_SA_PiSA_SB_
    .private_segment_fixed_size: 0
    .sgpr_count:     108
    .sgpr_spill_count: 0
    .symbol:         _Z6k_iterILb1ELb0EEvPKfS1_PKiPK15HIP_vector_typeIfLj4EES7_S1_S1_S3_S1_PfS8_S1_S3_PDF16_PS5_SA_PiSA_SB_.kd
    .uniform_work_group_size: 1
    .uses_dynamic_stack: false
    .vgpr_count:     256
    .vgpr_spill_count: 0
    .wavefront_size: 64
  - .agpr_count:     0
    .args:
      - .actual_access:  read_only
        .address_space:  global
        .offset:         0
        .size:           8
        .value_kind:     global_buffer
      - .actual_access:  read_only
        .address_space:  global
        .offset:         8
        .size:           8
        .value_kind:     global_buffer
      - .actual_access:  read_only
        .address_space:  global
        .offset:         16
        .size:           8
        .value_kind:     global_buffer
      - .actual_access:  read_only
        .address_space:  global
        .offset:         24
        .size:           8
        .value_kind:     global_buffer
      - .actual_access:  read_only
        .address_space:  global
        .offset:         32
        .size:           8
        .value_kind:     global_buffer
      - .actual_access:  read_only
        .address_space:  global
        .offset:         40
        .size:           8
        .value_kind:     global_buffer
      - .actual_access:  read_only
        .address_space:  global
        .offset:         48
        .size:           8
        .value_kind:     global_buffer
      - .actual_access:  read_only
        .address_space:  global
        .offset:         56
        .size:           8
        .value_kind:     global_buffer
      - .actual_access:  read_only
        .address_space:  global
        .offset:         64
        .size:           8
        .value_kind:     global_buffer
      - .address_space:  global
        .offset:         72
        .size:           8
        .value_kind:     global_buffer
      - .actual_access:  read_only
        .address_space:  global
        .offset:         80
        .size:           8
        .value_kind:     global_buffer
      - .actual_access:  read_only
        .address_space:  global
        .offset:         88
        .size:           8
        .value_kind:     global_buffer
      - .actual_access:  read_only
        .address_space:  global
        .offset:         96
        .size:           8
        .value_kind:     global_buffer
      - .actual_access:  read_only
        .address_space:  global
        .offset:         104
        .size:           8
        .value_kind:     global_buffer
      - .actual_access:  read_only
        .address_space:  global
        .offset:         112
        .size:           8
        .value_kind:     global_buffer
      - .actual_access:  read_only
        .address_space:  global
        .offset:         120
        .size:           8
        .value_kind:     global_buffer
      - .actual_access:  read_only
        .address_space:  global
        .offset:         128
        .size:           8
        .value_kind:     global_buffer
      - .actual_access:  read_only
        .address_space:  global
        .offset:         136
        .size:           8
        .value_kind:     global_buffer
      - .actual_access:  read_only
        .address_space:  global
        .offset:         144
        .size:           8
        .value_kind:     global_buffer
    .group_segment_fixed_size: 5808
    .kernarg_segment_align: 8
    .kernarg_segment_size: 152
    .language:       OpenCL C
    .language_version:
      - 2
      - 0
    .max_flat_workgroup_size: 512
    .name:           _Z6k_iterILb0ELb0EEvPKfS1_PKiPK15HIP_vector_typeIfLj4EES7_S1_S1_S3_S1_PfS8_S1_S3_PDF16_PS5_SA_PiSA_SB_
    .private_segment_fixed_size: 0
    .sgpr_count:     46
    .sgpr_spill_count: 0
    .symbol:         _Z6k_iterILb0ELb0EEvPKfS1_PKiPK15HIP_vector_typeIfLj4EES7_S1_S1_S3_S1_PfS8_S1_S3_PDF16_PS5_SA_PiSA_SB_.kd
    .uniform_work_group_size: 1
    .uses_dynamic_stack: false
    .vgpr_count:     184
    .vgpr_spill_count: 0
    .wavefront_size: 64
  - .agpr_count:     0
    .args:
      - .actual_access:  read_only
        .address_space:  global
        .offset:         0
        .size:           8
        .value_kind:     global_buffer
      - .actual_access:  read_only
        .address_space:  global
        .offset:         8
        .size:           8
        .value_kind:     global_buffer
      - .actual_access:  read_only
        .address_space:  global
        .offset:         16
        .size:           8
        .value_kind:     global_buffer
      - .actual_access:  read_only
        .address_space:  global
        .offset:         24
        .size:           8
        .value_kind:     global_buffer
      - .actual_access:  read_only
        .address_space:  global
        .offset:         32
        .size:           8
        .value_kind:     global_buffer
      - .actual_access:  read_only
        .address_space:  global
        .offset:         40
        .size:           8
        .value_kind:     global_buffer
      - .actual_access:  read_only
        .address_space:  global
        .offset:         48
        .size:           8
        .value_kind:     global_buffer
      - .actual_access:  read_only
        .address_space:  global
        .offset:         56
        .size:           8
        .value_kind:     global_buffer
      - .actual_access:  read_only
        .address_space:  global
        .offset:         64
        .size:           8
        .value_kind:     global_buffer
      - .address_space:  global
        .offset:         72
        .size:           8
        .value_kind:     global_buffer
      - .actual_access:  write_only
        .address_space:  global
        .offset:         80
        .size:           8
        .value_kind:     global_buffer
      - .actual_access:  read_only
        .address_space:  global
        .offset:         88
        .size:           8
        .value_kind:     global_buffer
      - .actual_access:  read_only
        .address_space:  global
        .offset:         96
        .size:           8
        .value_kind:     global_buffer
      - .actual_access:  read_only
        .address_space:  global
        .offset:         104
        .size:           8
        .value_kind:     global_buffer
      - .actual_access:  read_only
        .address_space:  global
        .offset:         112
        .size:           8
        .value_kind:     global_buffer
      - .actual_access:  read_only
        .address_space:  global
        .offset:         120
        .size:           8
        .value_kind:     global_buffer
      - .actual_access:  read_only
        .address_space:  global
        .offset:         128
        .size:           8
        .value_kind:     global_buffer
      - .actual_access:  read_only
        .address_space:  global
        .offset:         136
        .size:           8
        .value_kind:     global_buffer
      - .actual_access:  read_only
        .address_space:  global
        .offset:         144
        .size:           8
        .value_kind:     global_buffer
    .group_segment_fixed_size: 5808
    .kernarg_segment_align: 8
    .kernarg_segment_size: 152
    .language:       OpenCL C
    .language_version:
      - 2
      - 0
    .max_flat_workgroup_size: 512
    .name:           _Z6k_iterILb0ELb1EEvPKfS1_PKiPK15HIP_vector_typeIfLj4EES7_S1_S1_S3_S1_PfS8_S1_S3_PDF16_PS5_SA_PiSA_SB_
    .private_segment_fixed_size: 0
    .sgpr_count:     54
    .sgpr_spill_count: 0
    .symbol:         _Z6k_iterILb0ELb1EEvPKfS1_PKiPK15HIP_vector_typeIfLj4EES7_S1_S1_S3_S1_PfS8_S1_S3_PDF16_PS5_SA_PiSA_SB_.kd
    .uniform_work_group_size: 1
    .uses_dynamic_stack: false
    .vgpr_count:     184
    .vgpr_spill_count: 0
    .wavefront_size: 64
